# post row loop: all 16 row loads issued in one batch into unused registers (were three dependent batches = three memory round trips per row), counted vmcnt re-derived
# speedup vs baseline: 1.0030x; 1.0030x over previous
.LBB0_1141:
	s_waitcnt lgkmcnt(0)
	v_lshl_add_u64 v[50:51], s[40:41], 0, v[80:81]
	s_mov_b64 s[4:5], 0x40e00000
	v_lshl_add_u64 v[46:47], v[50:51], 0, s[4:5]
	v_add_co_u32_e32 v48, vcc, 0x40e00000, v50
	s_mov_b64 s[4:5], 0x42e00000
	s_nop 0
	v_addc_co_u32_e32 v49, vcc, 0, v51, vcc
	v_lshl_add_u64 v[52:53], v[50:51], 0, s[4:5]
	s_mov_b32 s4, 0x42e00000
	v_add_co_u32_e32 v50, vcc, s4, v50
	global_load_dwordx4 v[54:57], v[48:49], off nt
	s_nop 0
	global_load_dwordx4 v[46:49], v[46:47], off offset:16 nt
	v_addc_co_u32_e32 v51, vcc, 0, v51, vcc
	global_load_dwordx4 v[58:61], v[50:51], off nt
	s_nop 0
	global_load_dwordx4 v[50:53], v[52:53], off offset:16 nt
	v_lshl_add_u64 v[108:109], s[40:41], 0, v[76:77]
	s_mov_b64 s[4:5], 0x2e200000
	v_lshl_add_u64 v[156:157], s[40:41], 0, v[74:75]
	s_mov_b64 vcc, 0x2e200800
	v_lshl_add_u64 v[184:185], v[108:109], 0, vcc
	s_mov_b64 vcc, 0x36e01800
	v_lshl_add_u64 v[186:187], v[156:157], 0, vcc
	global_load_dwordx4 v[188:191], v[184:185], off offset:-2048 nt
	global_load_dwordx4 v[192:195], v[184:185], off offset:-2032 nt
	global_load_dwordx4 v[196:199], v[184:185], off nt
	global_load_dwordx4 v[200:203], v[184:185], off offset:16 nt
	global_load_dwordx4 v[204:207], v[184:185], off offset:2048 nt
	global_load_dwordx4 v[208:211], v[184:185], off offset:2064 nt
	global_load_dwordx4 v[212:215], v[186:187], off offset:-2048 nt
	global_load_dwordx4 v[216:219], v[186:187], off offset:-2032 nt
	global_load_dwordx4 v[220:223], v[186:187], off nt
	global_load_dwordx4 v[234:237], v[186:187], off offset:16 nt
	global_load_dwordx4 v[238:241], v[186:187], off offset:2048 nt
	global_load_dwordx4 v[242:245], v[186:187], off offset:2064 nt
	s_add_i32 s48, s48, s66
	v_lshl_add_u64 v[74:75], v[74:75], 0, s[6:7]
	v_lshl_add_u64 v[76:77], v[76:77], 0, s[10:11]
	v_lshl_add_u64 v[80:81], v[80:81], 0, s[22:23]
	s_cmpk_lt_i32 s48, 0x4000
	s_waitcnt vmcnt(15)
	v_lshlrev_b32_e32 v2, 16, v54
	v_and_b32_e32 v82, 0xffff0000, v54
	v_lshlrev_b32_e32 v86, 16, v55
	v_and_b32_e32 v127, 0xffff0000, v55
	v_lshl_add_u64 v[54:55], v[108:109], 0, s[4:5]
	s_mov_b32 s4, 0x2e200000
	s_waitcnt vmcnt(13)
	v_lshlrev_b32_e32 v4, 16, v58
	v_and_b32_e32 v72, 0xffff0000, v58
	v_add_co_u32_e32 v58, vcc, s4, v108
	v_lshlrev_b32_e32 v123, 16, v59
	v_and_b32_e32 v125, 0xffff0000, v59
	v_addc_co_u32_e32 v59, vcc, 0, v109, vcc
	s_mov_b32 s4, 0x2e201000
	v_add_co_u32_e32 v110, vcc, s4, v108
	s_mov_b64 s[4:5], 0x2e200800
	v_lshlrev_b32_e32 v131, 16, v60
	v_and_b32_e32 v133, 0xffff0000, v60
	v_lshlrev_b32_e32 v137, 16, v61
	v_and_b32_e32 v136, 0xffff0000, v61
	v_addc_co_u32_e32 v111, vcc, 0, v109, vcc
	v_lshl_add_u64 v[60:61], v[108:109], 0, s[4:5]
	s_mov_b64 s[4:5], 0x2e201000
	v_lshlrev_b32_e32 v135, 16, v57
	v_lshlrev_b32_e32 v129, 16, v56
	v_and_b32_e32 v134, 0xffff0000, v56
	v_and_b32_e32 v164, 0xffff0000, v57
	s_nop 0
	s_nop 0
	s_nop 0
	v_lshl_add_u64 v[112:113], v[108:109], 0, s[4:5]
	s_nop 0
	s_mov_b64 s[4:5], 0x36e01000
	v_lshl_add_u64 v[144:145], v[156:157], 0, s[4:5]
	s_mov_b32 s4, 0x36e01000
	v_add_co_u32_e32 v148, vcc, s4, v156
	s_mov_b32 s4, 0x36e02000
	s_nop 0
	v_addc_co_u32_e32 v149, vcc, 0, v157, vcc
	v_add_co_u32_e32 v158, vcc, s4, v156
	s_mov_b64 s[4:5], 0x36e01800
	s_nop 0
	v_addc_co_u32_e32 v159, vcc, 0, v157, vcc
	v_lshl_add_u64 v[152:153], v[156:157], 0, s[4:5]
	s_mov_b64 s[4:5], 0x36e02000
	v_lshl_add_u64 v[160:161], v[156:157], 0, s[4:5]
	v_add_f32_e32 v82, v72, v82
	v_add_f32_e32 v4, v4, v2
	v_add_f32_e32 v2, 0, v4
	v_add_f32_e32 v2, v82, v2
	v_add_f32_e32 v86, v123, v86
	v_add_f32_e32 v2, v86, v2
	v_add_f32_e32 v123, v125, v127
	v_add_f32_e32 v2, v123, v2
	v_add_f32_e32 v125, v131, v129
	v_add_f32_e32 v2, v125, v2
	s_waitcnt vmcnt(11)
	v_lshlrev_b32_e32 v165, 16, v188
	v_and_b32_e32 v166, 0xffff0000, v188
	s_waitcnt vmcnt(9)
	v_lshlrev_b32_e32 v169, 16, v196
	v_and_b32_e32 v170, 0xffff0000, v196
	s_waitcnt vmcnt(7)
	v_lshlrev_b32_e32 v132, 16, v204
	v_and_b32_e32 v130, 0xffff0000, v204
	v_lshlrev_b32_e32 v124, 16, v206
	v_and_b32_e32 v122, 0xffff0000, v206
	s_waitcnt vmcnt(6)
	v_lshlrev_b32_e32 v118, 16, v208
	v_and_b32_e32 v116, 0xffff0000, v208
	v_lshlrev_b32_e32 v114, 16, v209
	v_and_b32_e32 v112, 0xffff0000, v209
	v_lshlrev_b32_e32 v110, 16, v210
	v_and_b32_e32 v108, 0xffff0000, v210
	v_lshlrev_b32_e32 v66, 16, v211
	v_and_b32_e32 v62, 0xffff0000, v211
	s_nop 0
	s_nop 0
	s_nop 0
	s_nop 0
	s_nop 0
	v_lshlrev_b32_e32 v128, 16, v205
	v_and_b32_e32 v126, 0xffff0000, v205
	v_lshlrev_b32_e32 v84, 16, v207
	v_and_b32_e32 v120, 0xffff0000, v207
	v_lshlrev_b32_e32 v171, 16, v197
	v_lshlrev_b32_e32 v167, 16, v189
	v_and_b32_e32 v168, 0xffff0000, v195
	v_and_b32_e32 v172, 0xffff0000, v203
	s_waitcnt vmcnt(5)
	v_lshlrev_b32_e32 v173, 16, v212
	s_waitcnt vmcnt(3)
	v_lshlrev_b32_e32 v175, 16, v220
	v_and_b32_e32 v140, 0xffff0000, v212
	v_and_b32_e32 v148, 0xffff0000, v220
	s_waitcnt vmcnt(1)
	v_lshlrev_b32_e32 v179, 16, v238
	v_and_b32_e32 v180, 0xffff0000, v238
	v_add_f32_e32 v156, v173, v175
	v_add_f32_e32 v156, -2.0, v156
	v_add_f32_e32 v72, v140, v148
	v_fma_f32 v156, v14, v156, 2.0
	v_add_f32_e32 v72, -2.0, v72
	v_mul_f32_e32 v156, v156, v169
	v_fma_f32 v72, v15, v72, 2.0
	v_lshlrev_b32_e32 v174, 16, v213
	s_waitcnt vmcnt(0)
	v_lshlrev_b32_e32 v115, 16, v242
	v_and_b32_e32 v113, 0xffff0000, v242
	v_lshlrev_b32_e32 v111, 16, v243
	v_and_b32_e32 v109, 0xffff0000, v243
	v_mul_f32_e32 v156, v156, v165
	v_mul_f32_e32 v72, v72, v170
	v_lshlrev_b32_e32 v161, 16, v214
	v_and_b32_e32 v160, 0xffff0000, v213
	v_lshlrev_b32_e32 v141, 16, v222
	v_and_b32_e32 v140, 0xffff0000, v221
	v_lshlrev_b32_e32 v176, 16, v221
	v_lshlrev_b32_e32 v20, 16, v244
	v_and_b32_e32 v17, 0xffff0000, v244
	v_fma_f32 v162, v6, v156, 0
	v_mul_f32_e32 v72, v72, v166
	v_pk_add_f32 v[140:141], v[160:161], v[140:141]
	v_fmac_f32_e32 v162, v7, v72
	v_add_f32_e32 v72, v174, v176
	v_pk_add_f32 v[140:141], v[140:141], -2.0 op_sel_hi:[1,0]
	v_lshlrev_b32_e32 v70, 16, v240
	v_and_b32_e32 v121, 0xffff0000, v240
	v_lshlrev_b32_e32 v119, 16, v241
	v_and_b32_e32 v117, 0xffff0000, v241
	v_add_f32_e32 v72, -2.0, v72
	v_lshlrev_b32_e32 v159, 16, v198
	v_and_b32_e32 v158, 0xffff0000, v197
	v_pk_fma_f32 v[140:141], v[98:99], v[140:141], 2.0 op_sel_hi:[1,1,0]
	v_lshlrev_b32_e32 v181, 16, v239
	v_and_b32_e32 v182, 0xffff0000, v239
	v_fma_f32 v72, v16, v72, 2.0
	v_lshlrev_b32_e32 v157, 16, v190
	v_and_b32_e32 v156, 0xffff0000, v189
	v_pk_mul_f32 v[140:141], v[140:141], v[158:159]
	v_mul_f32_e32 v72, v72, v171
	v_pk_mul_f32 v[140:141], v[140:141], v[156:157]
	v_lshlrev_b32_e32 v157, 16, v215
	v_and_b32_e32 v156, 0xffff0000, v214
	v_lshlrev_b32_e32 v159, 16, v223
	v_and_b32_e32 v158, 0xffff0000, v222
	v_mul_f32_e32 v72, v72, v167
	v_pk_add_f32 v[156:157], v[156:157], v[158:159]
	v_fmac_f32_e32 v162, v8, v72
	v_pk_mul_f32 v[140:141], v[88:89], v[140:141]
	v_pk_add_f32 v[156:157], v[156:157], -2.0 op_sel_hi:[1,0]
	v_add_f32_e32 v63, v140, v162
	v_lshlrev_b32_e32 v149, 16, v199
	v_and_b32_e32 v148, 0xffff0000, v198
	v_pk_fma_f32 v[156:157], v[100:101], v[156:157], 2.0 op_sel_hi:[1,1,0]
	v_add_f32_e32 v63, v141, v63
	v_lshlrev_b32_e32 v141, 16, v191
	v_and_b32_e32 v140, 0xffff0000, v190
	v_pk_mul_f32 v[148:149], v[156:157], v[148:149]
	v_and_b32_e32 v64, 0xffff0000, v199
	v_lshlrev_b32_e32 v69, 16, v216
	v_and_b32_e32 v68, 0xffff0000, v215
	v_lshlrev_b32_e32 v143, 16, v234
	v_and_b32_e32 v142, 0xffff0000, v223
	v_pk_mul_f32 v[140:141], v[148:149], v[140:141]
	v_pk_add_f32 v[68:69], v[68:69], v[142:143]
	v_pk_mul_f32 v[140:141], v[90:91], v[140:141]
	v_pk_add_f32 v[68:69], v[68:69], -2.0 op_sel_hi:[1,0]
	v_add_f32_e32 v63, v140, v63
	v_and_b32_e32 v140, 0xffff0000, v191
	v_lshlrev_b32_e32 v65, 16, v200
	v_pk_fma_f32 v[68:69], v[102:103], v[68:69], 2.0 op_sel_hi:[1,1,0]
	v_add_f32_e32 v63, v141, v63
	v_lshlrev_b32_e32 v141, 16, v192
	v_pk_mul_f32 v[64:65], v[68:69], v[64:65]
	v_lshlrev_b32_e32 v143, 16, v217
	v_pk_mul_f32 v[64:65], v[64:65], v[140:141]
	v_and_b32_e32 v142, 0xffff0000, v216
	v_lshlrev_b32_e32 v149, 16, v235
	v_and_b32_e32 v148, 0xffff0000, v234
	v_pk_mul_f32 v[64:65], v[92:93], v[64:65]
	v_pk_add_f32 v[142:143], v[142:143], v[148:149]
	v_add_f32_e32 v63, v64, v63
	v_pk_add_f32 v[142:143], v[142:143], -2.0 op_sel_hi:[1,0]
	v_add_f32_e32 v63, v65, v63
	v_and_b32_e32 v64, 0xffff0000, v46
	v_lshlrev_b32_e32 v65, 16, v46
	v_and_b32_e32 v68, 0xffff0000, v50
	v_lshlrev_b32_e32 v69, 16, v50
	v_lshlrev_b32_e32 v141, 16, v201
	v_and_b32_e32 v140, 0xffff0000, v200
	v_pk_fma_f32 v[142:143], v[104:105], v[142:143], 2.0 op_sel_hi:[1,1,0]
	v_pk_add_f32 v[64:65], v[64:65], v[68:69]
	v_lshlrev_b32_e32 v69, 16, v193
	v_and_b32_e32 v68, 0xffff0000, v192
	v_pk_mul_f32 v[140:141], v[142:143], v[140:141]
	v_and_b32_e32 v54, 0xffff0000, v201
	v_pk_mul_f32 v[68:69], v[140:141], v[68:69]
	v_lshlrev_b32_e32 v59, 16, v218
	v_pk_mul_f32 v[68:69], v[94:95], v[68:69]
	v_and_b32_e32 v58, 0xffff0000, v217
	v_add_f32_e32 v46, v68, v63
	v_add_f32_e32 v63, v69, v46
	v_lshlrev_b32_e32 v69, 16, v236
	v_and_b32_e32 v68, 0xffff0000, v235
	v_pk_add_f32 v[58:59], v[58:59], v[68:69]
	v_and_b32_e32 v46, 0xffff0000, v47
	v_lshlrev_b32_e32 v47, 16, v47
	v_and_b32_e32 v50, 0xffff0000, v51
	v_lshlrev_b32_e32 v51, 16, v51
	v_pk_add_f32 v[58:59], v[58:59], -2.0 op_sel_hi:[1,0]
	v_pk_add_f32 v[50:51], v[46:47], v[50:51]
	v_and_b32_e32 v46, 0xffff0000, v193
	v_lshlrev_b32_e32 v55, 16, v202
	v_pk_fma_f32 v[58:59], v[106:107], v[58:59], 2.0 op_sel_hi:[1,1,0]
	v_lshlrev_b32_e32 v47, 16, v194
	v_pk_mul_f32 v[54:55], v[58:59], v[54:55]
	v_and_b32_e32 v177, 0xffff0000, v237
	v_pk_mul_f32 v[46:47], v[54:55], v[46:47]
	v_and_b32_e32 v54, 0xffff0000, v52
	v_pk_mul_f32 v[46:47], v[96:97], v[46:47]
	v_lshlrev_b32_e32 v55, 16, v52
	v_add_f32_e32 v46, v46, v63
	v_add_f32_e32 v63, v47, v46
	v_and_b32_e32 v46, 0xffff0000, v48
	v_lshlrev_b32_e32 v47, 16, v48
	v_pk_add_f32 v[58:59], v[46:47], v[54:55]
	v_lshlrev_b32_e32 v47, 16, v195
	v_and_b32_e32 v46, 0xffff0000, v194
	v_lshlrev_b32_e32 v55, 16, v203
	v_and_b32_e32 v54, 0xffff0000, v202
	v_lshlrev_b32_e32 v57, 16, v219
	v_and_b32_e32 v56, 0xffff0000, v218
	v_lshlrev_b32_e32 v61, 16, v237
	v_and_b32_e32 v60, 0xffff0000, v236
	v_pk_add_f32 v[56:57], v[56:57], v[60:61]
	v_and_b32_e32 v178, 0xffff0000, v219
	v_pk_add_f32 v[56:57], v[56:57], -2.0 op_sel_hi:[1,0]
	v_add_f32_e32 v150, v136, v164
	v_pk_fma_f32 v[56:57], v[18:19], v[56:57], 2.0 op_sel_hi:[1,1,0]
	v_and_b32_e32 v48, 0xffff0000, v53
	v_pk_mul_f32 v[54:55], v[56:57], v[54:55]
	v_add_f32_e32 v67, v133, v134
	v_pk_mul_f32 v[46:47], v[54:55], v[46:47]
	v_add_f32_e32 v2, v67, v2
	v_pk_mul_f32 v[46:47], v[10:11], v[46:47]
	v_lshlrev_b32_e32 v12, 16, v245
	v_add_f32_e32 v46, v46, v63
	v_add_f32_e32 v136, v47, v46
	v_and_b32_e32 v46, 0xffff0000, v49
	v_lshlrev_b32_e32 v47, 16, v49
	v_lshlrev_b32_e32 v49, 16, v53
	v_pk_add_f32 v[48:49], v[46:47], v[48:49]
	v_add_f32_e32 v46, v177, v178
	v_add_f32_e32 v46, -2.0, v46
	v_fma_f32 v46, v21, v46, 2.0
	v_mul_f32_e32 v46, v46, v172
	v_mul_f32_e32 v46, v46, v168
	v_mul_f32_e32 v134, v13, v46
	v_pk_add_f32 v[46:47], v[134:135], v[136:137]
	v_and_b32_e32 v9, 0xffff0000, v245
	v_add_f32_e32 v2, v47, v2
	v_add_f32_e32 v2, v150, v2
	v_add_f32_e32 v2, v65, v2
	v_add_f32_e32 v2, v64, v2
	v_add_f32_e32 v2, v51, v2
	v_add_f32_e32 v2, v50, v2
	v_add_f32_e32 v2, v59, v2
	v_add_f32_e32 v2, v58, v2
	v_add_f32_e32 v2, v49, v2
	v_add_f32_e32 v2, v48, v2
	s_nop 1
	v_mov_b32_dpp v52, v2 quad_perm:[1,0,3,2] row_mask:0xf bank_mask:0xf
	s_waitcnt lgkmcnt(0)
	v_add_f32_e32 v2, v2, v52
	s_nop 1
	v_mov_b32_dpp v52, v2 quad_perm:[2,3,0,1] row_mask:0xf bank_mask:0xf
	s_waitcnt lgkmcnt(0)
	v_add_f32_e32 v2, v2, v52
	v_mov_b32_dpp v52, v46 quad_perm:[1,0,3,2] row_mask:0xf bank_mask:0xf
	v_mul_f32_e32 v53, 0x3c800000, v2
	v_fmac_f32_e32 v82, 0xbc800000, v2
	v_fmac_f32_e32 v4, 0xbc800000, v2
	v_fmac_f32_e32 v86, 0xbc800000, v2
	s_waitcnt lgkmcnt(0)
	v_pk_add_f32 v[54:55], v[46:47], v[52:53]
	v_pk_add_f32 v[56:57], v[46:47], v[52:53] neg_lo:[0,1] neg_hi:[0,1]
	v_mul_f32_e32 v47, v82, v82
	v_fmac_f32_e32 v47, v4, v4
	v_fmac_f32_e32 v47, v86, v86
	v_fmac_f32_e32 v123, 0xbc800000, v2
	v_fmac_f32_e32 v47, v123, v123
	v_fmac_f32_e32 v125, 0xbc800000, v2
	v_fmac_f32_e32 v47, v125, v125
	v_fmac_f32_e32 v67, 0xbc800000, v2
	v_fmac_f32_e32 v47, v67, v67
	v_fmac_f32_e32 v47, v57, v57
	v_fmac_f32_e32 v150, 0xbc800000, v2
	v_fmac_f32_e32 v47, v150, v150
	v_fmamk_f32 v60, v2, 0xbc800000, v65
	v_fmac_f32_e32 v64, 0xbc800000, v2
	v_mov_b32_e32 v2, v53
	v_fmac_f32_e32 v47, v60, v60
	v_pk_add_f32 v[52:53], v[50:51], v[2:3] op_sel_hi:[1,0] neg_lo:[0,1] neg_hi:[0,1]
	v_fmac_f32_e32 v47, v64, v64
	v_pk_mul_f32 v[50:51], v[52:53], v[52:53]
	v_pk_add_f32 v[48:49], v[48:49], v[2:3] op_sel_hi:[1,0] neg_lo:[0,1] neg_hi:[0,1]
	v_add_f32_e32 v47, v51, v47
	v_add_f32_e32 v47, v50, v47
	v_pk_add_f32 v[50:51], v[58:59], v[2:3] op_sel_hi:[1,0] neg_lo:[0,1] neg_hi:[0,1]
	v_mov_b32_dpp v46, v54 quad_perm:[2,3,0,1] row_mask:0xf bank_mask:0xf
	v_pk_mul_f32 v[58:59], v[50:51], v[50:51]
	s_nop 0
	v_add_f32_e32 v47, v59, v47
	v_add_f32_e32 v47, v58, v47
	v_pk_mul_f32 v[58:59], v[48:49], v[48:49]
	s_nop 0
	v_add_f32_e32 v2, v59, v47
	v_add_f32_e32 v2, v58, v2
	s_nop 1
	v_mov_b32_dpp v47, v2 quad_perm:[1,0,3,2] row_mask:0xf bank_mask:0xf
	s_waitcnt lgkmcnt(0)
	v_add_f32_e32 v2, v2, v47
	s_nop 1
	v_mov_b32_dpp v47, v2 quad_perm:[2,3,0,1] row_mask:0xf bank_mask:0xf
	s_waitcnt lgkmcnt(0)
	v_add_f32_e32 v2, v2, v47
	v_mov_b32_e32 v47, 0x3a27c5ac
	v_fmamk_f32 v2, v2, 0x3c800000, v47
	v_cmp_gt_f32_e32 vcc, s82, v2
	v_mul_f32_e32 v47, 0x4f800000, v2
	s_nop 0
	v_cndmask_b32_e32 v2, v2, v47, vcc
	v_sqrt_f32_e32 v47, v2
	s_nop 0
	v_add_u32_e32 v58, -1, v47
	v_fma_f32 v59, -v58, v47, v2
	v_cmp_ge_f32_e64 s[38:39], 0, v59
	v_add_u32_e32 v59, 1, v47
	s_nop 0
	v_cndmask_b32_e64 v58, v47, v58, s[38:39]
	v_fma_f32 v47, -v59, v47, v2
	v_cmp_lt_f32_e64 s[38:39], 0, v47
	s_nop 1
	v_cndmask_b32_e64 v47, v58, v59, s[38:39]
	v_mul_f32_e32 v58, 0x37800000, v47
	v_cndmask_b32_e32 v47, v47, v58, vcc
	v_cmp_class_f32_e32 vcc, v2, v229
	s_nop 1
	v_cndmask_b32_e32 v2, v47, v2, vcc
	v_div_scale_f32 v47, s[4:5], v2, v2, 1.0
	v_rcp_f32_e32 v58, v47
	s_nop 0
	v_fma_f32 v59, -v47, v58, 1.0
	v_fmac_f32_e32 v58, v59, v58
	v_div_scale_f32 v59, vcc, 1.0, v2, 1.0
	v_mul_f32_e32 v61, v59, v58
	v_fma_f32 v63, -v47, v61, v59
	v_fmac_f32_e32 v61, v63, v58
	v_fma_f32 v47, -v47, v61, v59
	v_div_fmas_f32 v47, v47, v58, v61
	v_div_fixup_f32 v47, v47, v2, 1.0
	v_pk_add_f32 v[54:55], v[54:55], v[46:47]
	v_mul_f32_e32 v133, v4, v47
	v_pk_mul_f32 v[56:57], v[56:57], v[46:47]
	v_mov_b32_e32 v72, v54
	v_mov_b32_e32 v55, v57
	v_pk_mul_f32 v[56:57], v[72:73], v[132:133]
	v_mul_f32_e32 v131, v82, v47
	v_add_f32_e32 v2, v22, v57
	v_add_f32_e32 v2, v56, v2
	v_mul_f32_e32 v58, v2, v179
	v_mov_b32_e32 v2, v54
	v_pk_mul_f32 v[56:57], v[2:3], v[130:131]
	v_mul_f32_e32 v129, v86, v47
	v_add_f32_e32 v2, v23, v57
	v_mov_b32_e32 v82, v54
	v_add_f32_e32 v2, v56, v2
	v_pk_mul_f32 v[56:57], v[82:83], v[128:129]
	v_mul_f32_e32 v127, v123, v47
	v_add_f32_e32 v4, v24, v57
	v_add_f32_e32 v4, v56, v4
	v_mul_f32_e32 v59, v4, v181
	v_mov_b32_e32 v4, v54
	v_pk_mul_f32 v[56:57], v[4:5], v[126:127]
	v_mul_f32_e32 v125, v125, v47
	v_add_f32_e32 v4, v25, v57
	v_mov_b32_e32 v86, v54
	v_add_f32_e32 v4, v56, v4
	v_pk_mul_f32 v[56:57], v[86:87], v[124:125]
	v_mul_f32_e32 v123, v67, v47
	v_add_f32_e32 v46, v26, v57
	v_add_f32_e32 v46, v56, v46
	v_mul_f32_e32 v61, v46, v70
	v_mov_b32_e32 v70, v54
	v_pk_mul_f32 v[56:57], v[70:71], v[122:123]
	v_mul_f32_e32 v2, v2, v180
	v_add_f32_e32 v46, v27, v57
	v_add_f32_e32 v46, v56, v46
	v_pk_mul_f32 v[56:57], v[54:55], v[84:85]
	v_mul_f32_e32 v65, v46, v121
	v_add_f32_e32 v46, v28, v57
	v_mul_f32_e32 v121, v150, v47
	v_mov_b32_e32 v55, v38
	v_add_f32_e32 v46, v56, v46
	v_pk_mul_f32 v[56:57], v[54:55], v[120:121]
	v_mul_f32_e32 v68, v46, v119
	v_add_f32_e32 v46, v29, v57
	v_mul_f32_e32 v119, v60, v47
	v_mov_b32_e32 v55, v39
	v_add_f32_e32 v46, v56, v46
	v_pk_mul_f32 v[56:57], v[54:55], v[118:119]
	v_mul_f32_e32 v69, v46, v117
	v_add_f32_e32 v46, v30, v57
	v_mul_f32_e32 v117, v64, v47
	v_mov_b32_e32 v55, v40
	v_add_f32_e32 v46, v56, v46
	v_pk_mul_f32 v[56:57], v[54:55], v[116:117]
	v_mul_f32_e32 v60, v46, v115
	v_add_f32_e32 v46, v31, v57
	v_mul_f32_e32 v115, v53, v47
	v_mov_b32_e32 v55, v41
	v_add_f32_e32 v46, v56, v46
	v_pk_mul_f32 v[56:57], v[54:55], v[114:115]
	v_mul_f32_e32 v64, v46, v113
	v_add_f32_e32 v46, v32, v57
	v_mul_f32_e32 v113, v52, v47
	v_mov_b32_e32 v55, v42
	v_add_f32_e32 v46, v56, v46
	v_pk_mul_f32 v[52:53], v[54:55], v[112:113]
	v_mul_f32_e32 v70, v46, v111
	v_add_f32_e32 v46, v33, v53
	v_mul_f32_e32 v111, v51, v47
	v_mov_b32_e32 v55, v43
	v_add_f32_e32 v46, v52, v46
	v_pk_mul_f32 v[52:53], v[54:55], v[110:111]
	v_mul_f32_e32 v72, v46, v109
	v_add_f32_e32 v46, v34, v53
	v_mul_f32_e32 v109, v50, v47
	v_mov_b32_e32 v55, v44
	v_add_f32_e32 v46, v52, v46
	v_pk_mul_f32 v[50:51], v[54:55], v[108:109]
	v_mul_f32_e32 v20, v46, v20
	v_add_f32_e32 v46, v35, v51
	v_mul_f32_e32 v67, v49, v47
	v_mov_b32_e32 v55, v45
	v_add_f32_e32 v46, v50, v46
	v_pk_mul_f32 v[50:51], v[54:55], v[66:67]
	v_mul_f32_e32 v56, 0x41000000, v58
	v_mul_f32_e32 v57, 0x41000000, v2
	v_mul_f32_e32 v82, v46, v17
	v_add_f32_e32 v17, v36, v51
	v_mul_f32_e32 v63, v48, v47
	v_mov_b32_e32 v55, v0
	v_mul_f32_e32 v48, 0x41000000, v60
	v_mul_f32_e32 v49, 0x41000000, v64
	v_med3_f32 v58, v56, s33, v233
	v_med3_f32 v57, v57, s33, v233
	v_mov_b32_e32 v56, v1
	v_add_f32_e32 v17, v50, v17
	v_pk_mul_f32 v[46:47], v[54:55], v[62:63]
	v_cvt_pk_fp8_f32 v56, v58, v57
	v_med3_f32 v48, v48, s33, v233
	v_med3_f32 v49, v49, s33, v233
	v_mov_b32_e32 v58, v1
	v_mul_f32_e32 v51, v17, v12
	v_add_f32_e32 v12, v37, v47
	v_cvt_pk_fp8_f32 v58, v48, v49
	v_mul_f32_e32 v4, v4, v182
	v_add_f32_e32 v12, v46, v12
	v_mul_f32_e32 v46, v12, v9
	v_mul_f32_e32 v52, 0x41000000, v59
	v_mul_f32_e32 v9, 0x41000000, v70
	v_mul_f32_e32 v53, 0x41000000, v4
	v_mul_f32_e32 v12, 0x41000000, v72
	v_mul_f32_e32 v54, 0x41000000, v61
	v_mul_f32_e32 v17, 0x41000000, v20
	v_mul_f32_e32 v55, 0x41000000, v65
	v_mul_f32_e32 v20, 0x41000000, v82
	v_med3_f32 v52, v52, s33, v233
	v_med3_f32 v53, v53, s33, v233
	v_med3_f32 v9, v9, s33, v233
	v_med3_f32 v12, v12, s33, v233
	v_cvt_pk_fp8_f32 v56, v52, v53 op_sel:[0,0,1]
	v_med3_f32 v52, v54, s33, v233
	v_med3_f32 v53, v55, s33, v233
	v_mov_b32_e32 v57, v1
	v_cvt_pk_fp8_f32 v58, v9, v12 op_sel:[0,0,1]
	v_med3_f32 v9, v17, s33, v233
	v_med3_f32 v12, v20, s33, v233
	v_mov_b32_e32 v59, v1
	v_cvt_pk_fp8_f32 v57, v52, v53
	v_cvt_pk_fp8_f32 v59, v9, v12
	v_mul_f32_e32 v50, 0x41000000, v68
	v_mul_f32_e32 v2, 0x41000000, v51
	v_mul_f32_e32 v51, 0x41000000, v69
	v_mul_f32_e32 v4, 0x41000000, v46
	v_med3_f32 v50, v50, s33, v233
	v_med3_f32 v51, v51, s33, v233
	v_med3_f32 v2, v2, s33, v233
	v_med3_f32 v4, v4, s33, v233
	v_cvt_pk_fp8_f32 v57, v50, v51 op_sel:[0,0,1]
	v_cvt_pk_fp8_f32 v59, v2, v4 op_sel:[0,0,1]
	v_lshl_add_u64 v[46:47], s[40:41], 0, v[78:79]
	v_add_co_u32_e32 v46, vcc, 0x1d200000, v46
	v_lshl_add_u64 v[78:79], v[78:79], 0, s[22:23]
	s_nop 0
	v_addc_co_u32_e32 v47, vcc, 0, v47, vcc
	global_store_dwordx4 v[46:47], v[56:59], off offset:1024 sc1
	s_cbranch_scc1 .LBB0_1141
